# final RMSNorm row loop: counted wait, first row converts start after vmcnt(4), second row waits vmcnt(0) later
# baseline (speedup 1.0000x reference)
; __device__ __forceinline__ float f16_lo(unsigned u) { return (float)__builtin_bit_cast(h16x2, u)[0]; }
; __device__ __forceinline__ float f16_hi(unsigned u) { return (float)__builtin_bit_cast(h16x2, u)[1]; }
; #define GAS __attribute__((address_space(1)))
; __global__ void __launch_bounds__(NWAVES * 64, 2) mk_fwd(Args args) {
;     ...
;           for (; m < M; m += 2 * NGW) { f32x4 v[2][4]; float ss[2] = {0.f, 0.f};
; #pragma unroll
;               for (int r = 0; r < 2; ++r) { const GAS v2u* xr = (const GAS v2u*)(hx + (size_t)(m + r * NGW) * D) + ln;
; #pragma unroll
;                   for (int q = 0; q < 4; ++q) { const v2u hv = xr[64 * q]; v[r][q] = (f32x4){pg8::f16_lo(hv.x), pg8::f16_hi(hv.x), pg8::f16_lo(hv.y), pg8::f16_hi(hv.y)}; } }
; #pragma unroll
;               for (int r = 0; r < 2; ++r) {
; #pragma unroll
;                   for (int q = 0; q < 4; ++q) ss[r] += (v[r][q].x * v[r][q].x + v[r][q].y * v[r][q].y) + (v[r][q].z * v[r][q].z + v[r][q].w * v[r][q].w);
.LBB0_1358:
	s_ashr_i32 s61, s60, 31
	s_lshl_b64 s[2:3], s[60:61], 11
	s_add_u32 s2, s1, s2
	s_addc_u32 s3, s4, s3
	v_lshl_add_u64 v[16:17], s[2:3], 0, v[4:5]
	global_load_dwordx2 v[20:21], v[16:17], off
	global_load_dwordx2 v[22:23], v[16:17], off offset:512
	global_load_dwordx2 v[24:25], v[16:17], off offset:1024
	s_add_i32 s2, s54, s60
	global_load_dwordx2 v[26:27], v[16:17], off offset:1536
	s_ashr_i32 s3, s2, 31
	s_lshl_b64 s[8:9], s[2:3], 11
	s_add_u32 s8, s1, s8
	s_addc_u32 s9, s4, s9
	v_lshl_add_u64 v[28:29], s[8:9], 0, v[4:5]
	global_load_dwordx2 v[30:31], v[28:29], off
	global_load_dwordx2 v[32:33], v[28:29], off offset:512
	global_load_dwordx2 v[34:35], v[28:29], off offset:1024
	global_load_dwordx2 v[36:37], v[28:29], off offset:1536
	s_lshl_b64 s[8:9], s[60:61], 12
	s_lshl_b64 s[2:3], s[2:3], 12
	s_add_i32 s60, s60, s5
	s_cmpk_lt_i32 s60, 0x4000
	s_waitcnt vmcnt(4)
	v_cvt_f32_f16_e32 v28, v20
	v_cvt_f32_f16_sdwa v29, v20 dst_sel:DWORD dst_unused:UNUSED_PAD src0_sel:WORD_1
	v_cvt_f32_f16_e32 v20, v21
	v_cvt_f32_f16_sdwa v21, v21 dst_sel:DWORD dst_unused:UNUSED_PAD src0_sel:WORD_1
	v_cvt_f32_f16_e32 v40, v22
	v_cvt_f32_f16_sdwa v41, v22 dst_sel:DWORD dst_unused:UNUSED_PAD src0_sel:WORD_1
	v_cvt_f32_f16_e32 v22, v23
	v_cvt_f32_f16_sdwa v23, v23 dst_sel:DWORD dst_unused:UNUSED_PAD src0_sel:WORD_1
	v_cvt_f32_f16_e32 v42, v24
	v_cvt_f32_f16_sdwa v43, v24 dst_sel:DWORD dst_unused:UNUSED_PAD src0_sel:WORD_1
	v_cvt_f32_f16_e32 v24, v25
	v_cvt_f32_f16_sdwa v25, v25 dst_sel:DWORD dst_unused:UNUSED_PAD src0_sel:WORD_1
	v_cvt_f32_f16_e32 v44, v26
	v_cvt_f32_f16_sdwa v45, v26 dst_sel:DWORD dst_unused:UNUSED_PAD src0_sel:WORD_1
	v_cvt_f32_f16_e32 v26, v27
	v_cvt_f32_f16_sdwa v27, v27 dst_sel:DWORD dst_unused:UNUSED_PAD src0_sel:WORD_1
	s_waitcnt vmcnt(0)
	v_cvt_f32_f16_e32 v46, v30
	v_cvt_f32_f16_sdwa v47, v30 dst_sel:DWORD dst_unused:UNUSED_PAD src0_sel:WORD_1
	v_cvt_f32_f16_e32 v30, v31
	v_cvt_f32_f16_sdwa v31, v31 dst_sel:DWORD dst_unused:UNUSED_PAD src0_sel:WORD_1
	v_cvt_f32_f16_e32 v48, v32
	v_cvt_f32_f16_sdwa v49, v32 dst_sel:DWORD dst_unused:UNUSED_PAD src0_sel:WORD_1
	v_cvt_f32_f16_e32 v32, v33
	v_cvt_f32_f16_sdwa v33, v33 dst_sel:DWORD dst_unused:UNUSED_PAD src0_sel:WORD_1
	v_mov_b32_e32 v56, v29
	v_mov_b32_e32 v57, v21
	v_mov_b32_e32 v60, v41
	v_mov_b32_e32 v61, v23
	v_mov_b32_e32 v54, v28
	v_mov_b32_e32 v55, v20
	v_mov_b32_e32 v58, v40
	v_mov_b32_e32 v59, v22
	v_mul_f32_e32 v62, v43, v43
	v_mul_f32_e32 v64, v25, v25
	v_pk_mul_f32 v[56:57], v[56:57], v[56:57]
	v_pk_mul_f32 v[60:61], v[60:61], v[60:61]
	v_cvt_f32_f16_e32 v50, v34
	v_cvt_f32_f16_sdwa v51, v34 dst_sel:DWORD dst_unused:UNUSED_PAD src0_sel:WORD_1
	v_cvt_f32_f16_e32 v34, v35
	v_cvt_f32_f16_sdwa v35, v35 dst_sel:DWORD dst_unused:UNUSED_PAD src0_sel:WORD_1
	v_pk_mul_f32 v[68:69], v[26:27], v[26:27]
	v_pk_fma_f32 v[62:63], v[42:43], v[42:43], v[62:63] op_sel_hi:[1,1,0]
	v_pk_fma_f32 v[64:65], v[24:25], v[24:25], v[64:65] op_sel_hi:[1,1,0]
	v_pk_fma_f32 v[54:55], v[54:55], v[54:55], v[56:57]
	v_pk_fma_f32 v[56:57], v[58:59], v[58:59], v[60:61]
	v_cvt_f32_f16_e32 v52, v36
	v_cvt_f32_f16_sdwa v53, v36 dst_sel:DWORD dst_unused:UNUSED_PAD src0_sel:WORD_1
	v_cvt_f32_f16_e32 v36, v37
	v_cvt_f32_f16_sdwa v37, v37 dst_sel:DWORD dst_unused:UNUSED_PAD src0_sel:WORD_1
	v_pk_mul_f32 v[66:67], v[44:45], v[44:45]
	v_mov_b32_e32 v63, v68
	v_mov_b32_e32 v65, v69
	v_pk_add_f32 v[54:55], v[54:55], v[54:55] op_sel:[0,1] op_sel_hi:[1,0]
	v_pk_add_f32 v[56:57], v[56:57], v[56:57] op_sel:[0,1] op_sel_hi:[1,0]
	v_pk_add_f32 v[58:59], v[62:63], v[64:65]
	v_mov_b32_e32 v55, v66
	v_mov_b32_e32 v57, v67
	v_mov_b32_e32 v62, v47
	v_mov_b32_e32 v63, v31
	v_mov_b32_e32 v66, v49
	v_mov_b32_e32 v67, v33
	v_mov_b32_e32 v60, v46
	v_mov_b32_e32 v61, v30
	v_mov_b32_e32 v64, v48
	v_mov_b32_e32 v65, v32
	v_pk_add_f32 v[54:55], v[54:55], v[56:57]
	v_pk_mul_f32 v[56:57], v[62:63], v[62:63]
	v_pk_mul_f32 v[62:63], v[66:67], v[66:67]
	v_mul_f32_e32 v68, v51, v51
	v_mul_f32_e32 v70, v35, v35
	v_pk_add_f32 v[54:55], v[54:55], v[58:59]
	v_pk_fma_f32 v[56:57], v[60:61], v[60:61], v[56:57]
	v_pk_fma_f32 v[58:59], v[64:65], v[64:65], v[62:63]
	v_pk_fma_f32 v[66:67], v[50:51], v[50:51], v[68:69] op_sel_hi:[1,1,0]
	v_pk_add_f32 v[56:57], v[56:57], v[56:57] op_sel:[0,1] op_sel_hi:[1,0]
	v_pk_add_f32 v[58:59], v[58:59], v[58:59] op_sel:[0,1] op_sel_hi:[1,0]
	v_pk_fma_f32 v[60:61], v[34:35], v[34:35], v[70:71] op_sel_hi:[1,1,0]
	v_pk_mul_f32 v[62:63], v[52:53], v[52:53]
	v_pk_mul_f32 v[64:65], v[36:37], v[36:37]
	v_mov_b32_e32 v57, v62
	v_mov_b32_e32 v59, v63
	v_mov_b32_e32 v67, v64
	v_mov_b32_e32 v61, v65
	v_pk_add_f32 v[56:57], v[56:57], v[58:59]
	v_pk_add_f32 v[58:59], v[66:67], v[60:61]
	s_waitcnt lgkmcnt(0)
; #define GAS __attribute__((address_space(1)))
; __device__ __forceinline__ float wave_sum(float v, int lane) {
; #pragma unroll
;     for (int o = 1; o < 64; o <<= 1) v += __builtin_bit_cast(float, __builtin_amdgcn_ds_bpermute((lane ^ o) << 2, __builtin_bit_cast(int, v)));
;     return v;
; __global__ void __launch_bounds__(NWAVES * 64, 2) mk_fwd(Args args) {
;     ...
;               for (int r = 0; r < 2; ++r) {
; #pragma unroll
;                   for (int q = 0; q < 4; ++q) ss[r] += (v[r][q].x * v[r][q].x + v[r][q].y * v[r][q].y) + (v[r][q].z * v[r][q].z + v[r][q].w * v[r][q].w);
;                   const float rstd = rsqrtf(wave_sum(ss[r], ln) * (1.f / D) + EPS); GAS f32x4* o = (GAS f32x4*)(ap->out + (size_t)(m + r * NGW) * D) + ln;
; #pragma unroll
;                   for (int q = 0; q < 4; ++q) o[64 * q] = v[r][q] * rstd * gr[64 * q]; } } }
	v_lshl_add_u64 v[38:39], v[88:89], 0, s[8:9]
	v_pk_add_f32 v[56:57], v[56:57], v[58:59]
	v_mov_b32_e32 v59, v54
	v_mov_b32_e32 v58, v56
	v_mov_b32_e32 v54, v57
	v_pk_add_f32 v[54:55], v[58:59], v[54:55]
	ds_bpermute_b32 v57, v3, v55
	ds_bpermute_b32 v56, v3, v54
	s_waitcnt lgkmcnt(0)
	v_pk_add_f32 v[54:55], v[54:55], v[56:57]
	ds_bpermute_b32 v57, v10, v55
	ds_bpermute_b32 v56, v10, v54
	s_waitcnt lgkmcnt(0)
	v_pk_add_f32 v[54:55], v[54:55], v[56:57]
	ds_bpermute_b32 v57, v11, v55
	ds_bpermute_b32 v56, v11, v54
	s_waitcnt lgkmcnt(0)
	v_pk_add_f32 v[54:55], v[54:55], v[56:57]
	ds_bpermute_b32 v57, v12, v55
	ds_bpermute_b32 v56, v12, v54
	s_waitcnt lgkmcnt(0)
	v_pk_add_f32 v[54:55], v[54:55], v[56:57]
	ds_bpermute_b32 v57, v13, v55
	ds_bpermute_b32 v56, v13, v54
	s_waitcnt lgkmcnt(0)
	v_pk_add_f32 v[54:55], v[54:55], v[56:57]
	ds_bpermute_b32 v57, v14, v55
	ds_bpermute_b32 v56, v14, v54
	s_waitcnt lgkmcnt(0)
	v_pk_add_f32 v[54:55], v[54:55], v[56:57]
	s_nop 0
	v_pk_fma_f32 v[54:55], v[54:55], s[0:1], v[2:3] op_sel_hi:[1,0,0]
	s_nop 0
	v_mul_f32_e32 v15, 0x4b800000, v55
	v_cmp_gt_f32_e32 vcc, s6, v55
	s_nop 1
	v_cndmask_b32_e32 v15, v55, v15, vcc
	v_rsq_f32_e32 v15, v15
	s_nop 0
	v_mul_f32_e32 v55, 0x45800000, v15
	v_cndmask_b32_e32 v56, v15, v55, vcc
	v_pk_mul_f32 v[28:29], v[56:57], v[28:29] op_sel_hi:[0,1]
	v_pk_mul_f32 v[20:21], v[56:57], v[20:21] op_sel_hi:[0,1]
	v_pk_mul_f32 v[18:19], v[20:21], v[74:75]
	v_pk_mul_f32 v[16:17], v[28:29], v[72:73]
	global_store_dwordx4 v[38:39], v[16:19], off sc1
	v_pk_mul_f32 v[20:21], v[56:57], v[22:23] op_sel_hi:[0,1]
	v_pk_mul_f32 v[22:23], v[56:57], v[40:41] op_sel_hi:[0,1]
	v_mul_f32_e32 v15, 0x4b800000, v54
	v_cmp_gt_f32_e32 vcc, s6, v54
	v_pk_mul_f32 v[90:91], v[22:23], v[76:77]
	v_pk_mul_f32 v[92:93], v[20:21], v[78:79]
	global_store_dwordx4 v[38:39], v[90:93], off offset:1024 sc1
	v_pk_mul_f32 v[20:21], v[56:57], v[24:25] op_sel_hi:[0,1]
	v_pk_mul_f32 v[22:23], v[56:57], v[42:43] op_sel_hi:[0,1]
	v_cndmask_b32_e32 v15, v54, v15, vcc
	v_rsq_f32_e32 v15, v15
	v_pk_mul_f32 v[94:95], v[22:23], v[80:81]
	v_pk_mul_f32 v[96:97], v[20:21], v[82:83]
	global_store_dwordx4 v[38:39], v[94:97], off offset:2048 sc1
	v_pk_mul_f32 v[20:21], v[56:57], v[26:27] op_sel_hi:[0,1]
	v_pk_mul_f32 v[22:23], v[56:57], v[44:45] op_sel_hi:[0,1]
	v_pk_mul_f32 v[98:99], v[22:23], v[84:85]
	v_pk_mul_f32 v[100:101], v[20:21], v[86:87]
	global_store_dwordx4 v[38:39], v[98:101], off offset:3072 sc1
	v_mul_f32_e32 v22, 0x45800000, v15
	v_cndmask_b32_e32 v22, v15, v22, vcc
	v_pk_mul_f32 v[24:25], v[22:23], v[30:31] op_sel_hi:[0,1]
	v_pk_mul_f32 v[26:27], v[22:23], v[46:47] op_sel_hi:[0,1]
	v_lshl_add_u64 v[20:21], v[88:89], 0, s[2:3]
	v_pk_mul_f32 v[102:103], v[26:27], v[72:73]
	v_pk_mul_f32 v[104:105], v[24:25], v[74:75]
	global_store_dwordx4 v[20:21], v[102:105], off sc1
	v_pk_mul_f32 v[24:25], v[22:23], v[32:33] op_sel_hi:[0,1]
	v_pk_mul_f32 v[26:27], v[22:23], v[48:49] op_sel_hi:[0,1]
	v_pk_mul_f32 v[106:107], v[26:27], v[76:77]
	v_pk_mul_f32 v[108:109], v[24:25], v[78:79]
	global_store_dwordx4 v[20:21], v[106:109], off offset:1024 sc1
	v_pk_mul_f32 v[24:25], v[22:23], v[34:35] op_sel_hi:[0,1]
	v_pk_mul_f32 v[26:27], v[22:23], v[50:51] op_sel_hi:[0,1]
	v_pk_mul_f32 v[110:111], v[26:27], v[80:81]
	v_pk_mul_f32 v[112:113], v[24:25], v[82:83]
	global_store_dwordx4 v[20:21], v[110:113], off offset:2048 sc1
	v_pk_mul_f32 v[24:25], v[22:23], v[36:37] op_sel_hi:[0,1]
	v_pk_mul_f32 v[22:23], v[22:23], v[52:53] op_sel_hi:[0,1]
	v_pk_mul_f32 v[114:115], v[22:23], v[84:85]
	v_pk_mul_f32 v[116:117], v[24:25], v[86:87]
	global_store_dwordx4 v[20:21], v[114:117], off offset:3072 sc1
	s_cbranch_scc1 .LBB0_1358
